# v5 + mLSTM chain: static priority raise (s_setprio 1) for waves 4..7 of the chain workgroups, reset at the end of P7
# speedup vs baseline: 1.0076x; 1.0053x over previous
.LBB0_2123:
	s_and_b64 vcc, exec, s[0:1]
	s_cbranch_vccz .LBB0_2197
	v_readfirstlane_b32 s98, v0
	s_bitcmp1_b32 s98, 8
	s_cbranch_scc0 .Lml_noprio
	s_setprio 1
.Lml_noprio:
	s_waitcnt lgkmcnt(0)
	s_barrier
	s_movk_i32 s0, 0x2940
	v_cmp_gt_i32_e32 vcc, s0, v152
	s_waitcnt vmcnt(0)
	v_lshl_add_u32 v2, v152, 2, 0
	s_and_saveexec_b64 s[0:1], vcc
	s_cbranch_execz .LBB0_2127
	v_add_u32_e32 v3, 0xfffffe00, v152
	v_add_u32_e32 v4, 0x10000, v2
	s_mov_b64 s[4:5], 0
	v_mov_b32_e32 v5, 0
	s_movk_i32 s2, 0x273f
